# speedup vs baseline: 1.0905x; 1.0143x over previous
.LBB1_3:
	s_or_b64 exec, exec, s[6:7]
	s_load_dwordx2 s[6:7], s[0:1], 0x8
	v_and_b32_e32 v79, 63, v0
	v_lshrrev_b32_e32 v103, 6, v0
	v_mov_b32_e32 v67, 0
	v_lshl_or_b32 v77, s2, 3, v103
	v_lshlrev_b32_e32 v74, 4, v79
	v_mov_b32_e32 v75, v67
	v_lshlrev_b32_e32 v66, 14, v77
	s_waitcnt lgkmcnt(0)
	v_lshl_add_u64 v[2:3], s[4:5], 0, v[74:75]
	v_lshl_add_u64 v[2:3], v[2:3], 0, v[66:67]
	s_movk_i32 s3, 0x1000
	v_add_co_u32_e32 v68, vcc, s3, v2
	s_movk_i32 s3, 0x2000
	s_nop 0
	v_addc_co_u32_e32 v69, vcc, 0, v3, vcc
	v_add_co_u32_e32 v70, vcc, s3, v2
	s_movk_i32 s3, 0x3000
	s_nop 0
	v_addc_co_u32_e32 v71, vcc, 0, v3, vcc
	v_add_co_u32_e32 v72, vcc, s3, v2
	v_and_b32_e32 v96, 63, v0
	v_lshlrev_b32_e32 v96, 7, v96
	v_lshrrev_b32_e32 v97, 7, v0
	v_lshl_add_u32 v96, v97, 5, v96
	v_bfe_u32 v97, v0, 6, 1
	v_lshl_add_u32 v96, v97, 4, v96
	global_load_dwordx4 v[80:83], v96, s[6:7]
	v_add_u32_e32 v97, 0x2000, v96
	global_load_dwordx4 v[84:87], v97, s[6:7]
	v_add_u32_e32 v97, 0x4000, v96
	global_load_dwordx4 v[88:91], v97, s[6:7]
	v_add_u32_e32 v97, 0x6000, v96
	global_load_dwordx4 v[92:95], v97, s[6:7]
	global_load_dwordx4 v[62:65], v[2:3], off nt
	global_load_dwordx4 v[58:61], v[2:3], off offset:1024 nt
	global_load_dwordx4 v[54:57], v[2:3], off offset:2048 nt
	global_load_dwordx4 v[50:53], v[2:3], off offset:3072 nt
	global_load_dwordx4 v[30:33], v[70:71], off nt
	global_load_dwordx4 v[26:29], v[70:71], off offset:1024 nt
	global_load_dwordx4 v[22:25], v[70:71], off offset:2048 nt
	global_load_dwordx4 v[18:21], v[70:71], off offset:3072 nt
	v_addc_co_u32_e32 v73, vcc, 0, v3, vcc
	global_load_dwordx4 v[42:45], v[68:69], off offset:1024 nt
	global_load_dwordx4 v[38:41], v[68:69], off offset:2048 nt
	global_load_dwordx4 v[34:37], v[68:69], off offset:3072 nt
	global_load_dwordx4 v[14:17], v[72:73], off nt
	global_load_dwordx4 v[10:13], v[72:73], off offset:1024 nt
	global_load_dwordx4 v[6:9], v[72:73], off offset:2048 nt
	global_load_dwordx4 v[46:49], v[70:71], off offset:-4096 nt
	global_load_dwordx4 v[2:5], v[72:73], off offset:3072 nt
	s_load_dwordx2 s[6:7], s[0:1], 0x8
	s_load_dwordx2 s[4:5], s[0:1], 0x18
	v_lshrrev_b32_e32 v68, 7, v0
	v_or_b32_e32 v69, 0xfffffe00, v0
	v_lshrrev_b32_e32 v70, 1, v0
	v_lshlrev_b32_e32 v71, 2, v0
	v_lshrrev_b32_e32 v72, 4, v0
	v_lshlrev_b32_e32 v73, 4, v0
	s_mov_b64 s[8:9], 0
	s_movk_i32 s3, 0x5ff
	v_mov_b32_e32 v1, 0
	v_lshlrev_b32_e32 v76, 2, v79
.LBB1_4:
	s_waitcnt vmcnt(19)
	v_max3_f32 v1, v1, |v80|, |v81|
	ds_write_b128 v73, v[80:83]
	v_max3_f32 v1, v1, |v82|, |v83|
	s_waitcnt vmcnt(18)
	v_max3_f32 v1, v1, |v84|, |v85|
	ds_write_b128 v73, v[84:87] offset:8192
	v_max3_f32 v1, v1, |v86|, |v87|
	s_waitcnt vmcnt(17)
	v_max3_f32 v1, v1, |v88|, |v89|
	ds_write_b128 v73, v[88:91] offset:16384
	v_max3_f32 v1, v1, |v90|, |v91|
	s_waitcnt vmcnt(16)
	v_max3_f32 v1, v1, |v92|, |v93|
	ds_write_b128 v73, v[92:95] offset:24576
	v_max3_f32 v1, v1, |v94|, |v95|
	v_mbcnt_lo_u32_b32 v66, -1, 0
	v_mbcnt_hi_u32_b32 v66, -1, v66
	v_and_b32_e32 v67, 64, v66
	v_add_u32_e32 v67, 64, v67
	v_xor_b32_e32 v68, 32, v66
	v_cmp_lt_i32_e32 vcc, v68, v67
	v_xor_b32_e32 v69, 16, v66
	s_nop 0
	v_cndmask_b32_e32 v68, v66, v68, vcc
	v_lshlrev_b32_e32 v99, 2, v68
	ds_bpermute_b32 v68, v99, v1
	v_max_f32_e32 v1, v1, v1
	v_cmp_lt_i32_e32 vcc, v69, v67
	s_waitcnt lgkmcnt(0)
	v_max_f32_e32 v68, v68, v68
	v_max_f32_e32 v1, v1, v68
	v_cndmask_b32_e32 v68, v66, v69, vcc
	v_lshlrev_b32_e32 v98, 2, v68
	ds_bpermute_b32 v68, v98, v1
	v_xor_b32_e32 v69, 8, v66
	v_cmp_lt_i32_e32 vcc, v69, v67
	s_waitcnt lgkmcnt(0)
	v_max_f32_e32 v68, v68, v68
	v_max_f32_e32 v1, v1, v68
	v_cndmask_b32_e32 v68, v66, v69, vcc
	v_lshlrev_b32_e32 v97, 2, v68
	ds_bpermute_b32 v68, v97, v1
	v_xor_b32_e32 v69, 4, v66
	v_cmp_lt_i32_e32 vcc, v69, v67
	s_waitcnt lgkmcnt(0)
	v_max_f32_e32 v68, v68, v68
	v_max_f32_e32 v1, v1, v68
	v_cndmask_b32_e32 v68, v66, v69, vcc
	v_lshlrev_b32_e32 v96, 2, v68
	ds_bpermute_b32 v68, v96, v1
	v_xor_b32_e32 v69, 2, v66
	v_cmp_lt_i32_e32 vcc, v69, v67
	s_waitcnt lgkmcnt(0)
	v_max_f32_e32 v68, v68, v68
	v_max_f32_e32 v1, v1, v68
	v_cndmask_b32_e32 v68, v66, v69, vcc
	v_lshlrev_b32_e32 v75, 2, v68
	ds_bpermute_b32 v68, v75, v1
	v_xor_b32_e32 v69, 1, v66
	v_cmp_lt_i32_e32 vcc, v69, v67
	s_waitcnt lgkmcnt(0)
	v_max_f32_e32 v68, v68, v68
	v_max_f32_e32 v68, v1, v68
	v_cndmask_b32_e32 v1, v66, v69, vcc
	v_lshlrev_b32_e32 v1, 2, v1
	ds_bpermute_b32 v66, v1, v68
	v_cmp_eq_u32_e32 vcc, 0, v79
	s_waitcnt lgkmcnt(0)
	v_max_f32_e32 v66, v66, v66
	v_max_f32_e32 v78, v68, v66
	s_and_saveexec_b64 s[6:7], vcc
	v_lshlrev_b32_e32 v66, 2, v103
	ds_write_b32 v66, v78 offset:32896
	s_or_b64 exec, exec, s[6:7]
	v_mov_b32_e32 v85, 0
	s_waitcnt vmcnt(0) lgkmcnt(0)
	s_barrier
	ds_read_b128 v[70:73], v85 offset:32896
	ds_read_b128 v[66:69], v85 offset:32912
	ds_read_b128 v[80:83], v74
	v_lshlrev_b32_e32 v84, 1, v76
	v_lshlrev_b32_e32 v88, 13, v77
	v_lshl_add_u64 v[76:77], s[4:5], 0, v[84:85]
	v_mov_b32_e32 v89, v85
	ds_read_b128 v[84:87], v74 offset:1024
	v_lshl_add_u64 v[76:77], v[76:77], 0, v[88:89]
	s_waitcnt lgkmcnt(1)
	v_pk_fma_f32 v[88:89], v[80:81], v[62:63], 0 op_sel_hi:[1,0,0]
	v_pk_fma_f32 v[90:91], v[82:83], v[62:63], 0 op_sel_hi:[1,0,0]
	ds_read_b128 v[80:83], v74 offset:2048
	s_waitcnt lgkmcnt(1)
	v_pk_fma_f32 v[92:93], v[62:63], v[84:85], 0 op_sel_hi:[0,1,0]
	v_pk_fma_f32 v[94:95], v[62:63], v[86:87], 0 op_sel_hi:[0,1,0]
	ds_read_b128 v[84:87], v74 offset:3072
	v_add_f32_e64 v102, |v62|, |v63|
	s_waitcnt lgkmcnt(1)
	v_pk_fma_f32 v[104:105], v[80:81], v[62:63], v[88:89] op_sel:[0,1,0]
	v_pk_fma_f32 v[106:107], v[82:83], v[62:63], v[90:91] op_sel:[0,1,0]
	ds_read_b128 v[80:83], v74 offset:4096
	ds_read_b128 v[88:91], v74 offset:5120
	s_waitcnt lgkmcnt(2)
	v_pk_fma_f32 v[84:85], v[62:63], v[84:85], v[92:93] op_sel:[1,0,0]
	v_pk_fma_f32 v[86:87], v[62:63], v[86:87], v[94:95] op_sel:[1,0,0]
	v_add_f32_e64 v108, v102, |v64|
	s_waitcnt lgkmcnt(1)
	v_pk_fma_f32 v[92:93], v[80:81], v[64:65], v[104:105] op_sel_hi:[1,0,1]
	v_pk_fma_f32 v[94:95], v[82:83], v[64:65], v[106:107] op_sel_hi:[1,0,1]
	s_waitcnt lgkmcnt(0)
	v_pk_fma_f32 v[88:89], v[64:65], v[88:89], v[84:85] op_sel_hi:[0,1,1]
	ds_read_b128 v[80:83], v74 offset:6144
	v_pk_fma_f32 v[90:91], v[64:65], v[90:91], v[86:87] op_sel_hi:[0,1,1]
	ds_read_b128 v[84:87], v74 offset:7168
	v_mov_b32_e32 v102, v65
	v_add_f32_e64 v104, v108, |v65|
	s_waitcnt lgkmcnt(1)
	v_pk_fma_f32 v[92:93], v[80:81], v[102:103], v[92:93] op_sel_hi:[1,0,1]
	v_pk_fma_f32 v[94:95], v[82:83], v[102:103], v[94:95] op_sel_hi:[1,0,1]
	s_waitcnt lgkmcnt(0)
	v_pk_fma_f32 v[88:89], v[102:103], v[84:85], v[88:89] op_sel_hi:[0,1,1]
	v_cvt_pk_f16_f32 v85, v64, v65
	ds_read_b128 v[80:83], v74 offset:8192
	v_cvt_pk_f16_f32 v84, v62, v63
	v_pk_fma_f32 v[90:91], v[102:103], v[86:87], v[90:91] op_sel_hi:[0,1,1]
	global_store_dwordx2 v[76:77], v[84:85], off
	ds_read_b128 v[84:87], v74 offset:9216
	s_waitcnt lgkmcnt(1)
	v_pk_fma_f32 v[92:93], v[80:81], v[58:59], v[92:93] op_sel_hi:[1,0,1]
	v_pk_fma_f32 v[94:95], v[82:83], v[58:59], v[94:95] op_sel_hi:[1,0,1]
	ds_read_b128 v[80:83], v74 offset:10240
	v_add_f32_e64 v102, v104, |v58|
	s_waitcnt lgkmcnt(1)
	v_pk_fma_f32 v[88:89], v[58:59], v[84:85], v[88:89] op_sel_hi:[0,1,1]
	v_pk_fma_f32 v[104:105], v[58:59], v[86:87], v[90:91] op_sel_hi:[0,1,1]
	ds_read_b128 v[84:87], v74 offset:11264
	s_waitcnt lgkmcnt(1)
	v_pk_fma_f32 v[92:93], v[80:81], v[58:59], v[92:93] op_sel:[0,1,0]
	v_pk_fma_f32 v[94:95], v[82:83], v[58:59], v[94:95] op_sel:[0,1,0]
	ds_read_b128 v[80:83], v74 offset:12288
	v_lshrrev_b32_e32 v100, 3, v79
	s_waitcnt lgkmcnt(1)
	v_pk_fma_f32 v[84:85], v[58:59], v[84:85], v[88:89] op_sel:[1,0,0]
	ds_read_b128 v[88:91], v74 offset:13312
	v_pk_fma_f32 v[86:87], v[58:59], v[86:87], v[104:105] op_sel:[1,0,0]
	s_waitcnt lgkmcnt(1)
	v_pk_fma_f32 v[92:93], v[80:81], v[60:61], v[92:93] op_sel_hi:[1,0,1]
	v_pk_fma_f32 v[94:95], v[82:83], v[60:61], v[94:95] op_sel_hi:[1,0,1]
	ds_read_b128 v[80:83], v74 offset:14336
	s_waitcnt lgkmcnt(1)
	v_pk_fma_f32 v[88:89], v[60:61], v[88:89], v[84:85] op_sel_hi:[0,1,1]
	v_pk_fma_f32 v[90:91], v[60:61], v[90:91], v[86:87] op_sel_hi:[0,1,1]
	ds_read_b128 v[84:87], v74 offset:15360
	v_lshlrev_b32_e32 v79, 2, v100
	v_add_f32_e64 v102, v102, |v59|
	global_load_dword v101, v79, s[20:21]
	v_add_f32_e64 v104, v102, |v60|
	v_mov_b32_e32 v102, v61
	s_waitcnt lgkmcnt(1)
	v_pk_fma_f32 v[92:93], v[80:81], v[102:103], v[92:93] op_sel_hi:[1,0,1]
	v_pk_fma_f32 v[94:95], v[82:83], v[102:103], v[94:95] op_sel_hi:[1,0,1]
	ds_read_b128 v[80:83], v74 offset:16384
	s_waitcnt lgkmcnt(1)
	v_pk_fma_f32 v[88:89], v[102:103], v[84:85], v[88:89] op_sel_hi:[0,1,1]
	v_pk_fma_f32 v[90:91], v[102:103], v[86:87], v[90:91] op_sel_hi:[0,1,1]
	ds_read_b128 v[84:87], v74 offset:17408
	v_add_f32_e64 v104, v104, |v61|
	s_waitcnt lgkmcnt(1)
	v_pk_fma_f32 v[92:93], v[80:81], v[54:55], v[92:93] op_sel_hi:[1,0,1]
	v_pk_fma_f32 v[94:95], v[82:83], v[54:55], v[94:95] op_sel_hi:[1,0,1]
	ds_read_b128 v[80:83], v74 offset:18432
	v_add_f32_e64 v102, v104, |v54|
	s_waitcnt lgkmcnt(1)
	v_pk_fma_f32 v[88:89], v[54:55], v[84:85], v[88:89] op_sel_hi:[0,1,1]
	v_pk_fma_f32 v[104:105], v[54:55], v[86:87], v[90:91] op_sel_hi:[0,1,1]
	ds_read_b128 v[84:87], v74 offset:19456
	s_waitcnt lgkmcnt(1)
	v_pk_fma_f32 v[92:93], v[80:81], v[54:55], v[92:93] op_sel:[0,1,0]
	v_pk_fma_f32 v[94:95], v[82:83], v[54:55], v[94:95] op_sel:[0,1,0]
	ds_read_b128 v[80:83], v74 offset:20480
	v_add_f32_e64 v102, v102, |v55|
	s_waitcnt lgkmcnt(1)
	v_pk_fma_f32 v[84:85], v[54:55], v[84:85], v[88:89] op_sel:[1,0,0]
	ds_read_b128 v[88:91], v74 offset:21504
	v_pk_fma_f32 v[86:87], v[54:55], v[86:87], v[104:105] op_sel:[1,0,0]
	s_waitcnt lgkmcnt(1)
	v_pk_fma_f32 v[92:93], v[80:81], v[56:57], v[92:93] op_sel_hi:[1,0,1]
	v_pk_fma_f32 v[94:95], v[82:83], v[56:57], v[94:95] op_sel_hi:[1,0,1]
	ds_read_b128 v[80:83], v74 offset:22528
	s_waitcnt lgkmcnt(1)
	v_pk_fma_f32 v[104:105], v[56:57], v[88:89], v[84:85] op_sel_hi:[0,1,1]
	v_pk_fma_f32 v[106:107], v[56:57], v[90:91], v[86:87] op_sel_hi:[0,1,1]
	ds_read_b128 v[84:87], v74 offset:23552
	ds_read_b128 v[88:91], v74 offset:24576
	v_add_f32_e64 v108, v102, |v56|
	v_mov_b32_e32 v102, v57
	s_waitcnt lgkmcnt(2)
	v_pk_fma_f32 v[92:93], v[80:81], v[102:103], v[92:93] op_sel_hi:[1,0,1]
	v_pk_fma_f32 v[94:95], v[82:83], v[102:103], v[94:95] op_sel_hi:[1,0,1]
	ds_read_b128 v[80:83], v74 offset:25600
	s_waitcnt lgkmcnt(2)
	v_pk_fma_f32 v[104:105], v[102:103], v[84:85], v[104:105] op_sel_hi:[0,1,1]
	v_pk_fma_f32 v[106:107], v[102:103], v[86:87], v[106:107] op_sel_hi:[0,1,1]
	s_waitcnt lgkmcnt(1)
	v_pk_fma_f32 v[92:93], v[88:89], v[50:51], v[92:93] op_sel_hi:[1,0,1]
	ds_read_b128 v[84:87], v74 offset:26624
	v_pk_fma_f32 v[94:95], v[90:91], v[50:51], v[94:95] op_sel_hi:[1,0,1]
	ds_read_b128 v[88:91], v74 offset:27648
	s_waitcnt lgkmcnt(2)
	v_pk_fma_f32 v[80:81], v[50:51], v[80:81], v[104:105] op_sel_hi:[0,1,1]
	v_add_f32_e64 v114, v108, |v57|
	v_pk_fma_f32 v[104:105], v[50:51], v[82:83], v[106:107] op_sel_hi:[0,1,1]
	s_waitcnt lgkmcnt(1)
	v_pk_fma_f32 v[106:107], v[84:85], v[50:51], v[92:93] op_sel:[0,1,0]
	v_pk_fma_f32 v[108:109], v[86:87], v[50:51], v[94:95] op_sel:[0,1,0]
	s_waitcnt lgkmcnt(0)
	v_pk_fma_f32 v[110:111], v[50:51], v[88:89], v[80:81] op_sel:[1,0,0]
	ds_read_b128 v[80:83], v74 offset:28672
	ds_read_b128 v[84:87], v74 offset:29696
	v_pk_fma_f32 v[104:105], v[50:51], v[90:91], v[104:105] op_sel:[1,0,0]
	ds_read_b128 v[88:91], v74 offset:30720
	ds_read_b128 v[92:95], v74 offset:31744
	v_and_b32_e32 v79, 32, v0
	s_waitcnt lgkmcnt(3)
	v_pk_fma_f32 v[80:81], v[80:81], v[52:53], v[106:107] op_sel_hi:[1,0,1]
	s_waitcnt lgkmcnt(2)
	v_pk_fma_f32 v[84:85], v[52:53], v[84:85], v[110:111] op_sel_hi:[0,1,1]
	v_mov_b32_e32 v102, v53
	s_waitcnt lgkmcnt(1)
	v_pk_fma_f32 v[80:81], v[88:89], v[102:103], v[80:81] op_sel_hi:[1,0,1]
	s_waitcnt lgkmcnt(0)
	v_pk_fma_f32 v[84:85], v[102:103], v[92:93], v[84:85] op_sel_hi:[0,1,1]
	v_cmp_eq_u32_e64 s[8:9], 0, v79
	v_pk_fma_f32 v[82:83], v[82:83], v[52:53], v[108:109] op_sel_hi:[1,0,1]
	v_pk_fma_f32 v[86:87], v[52:53], v[86:87], v[104:105] op_sel_hi:[0,1,1]
	v_cndmask_b32_e64 v79, v84, v80, s[8:9]
	v_cndmask_b32_e64 v80, v80, v84, s[8:9]
	ds_bpermute_b32 v80, v99, v80
	v_pk_fma_f32 v[82:83], v[90:91], v[102:103], v[82:83] op_sel_hi:[1,0,1]
	v_pk_fma_f32 v[86:87], v[102:103], v[94:95], v[86:87] op_sel_hi:[0,1,1]
	v_cndmask_b32_e64 v84, v82, v86, s[8:9]
	ds_bpermute_b32 v84, v99, v84
	s_waitcnt lgkmcnt(1)
	v_add_f32_e32 v79, v79, v80
	v_cndmask_b32_e64 v80, v85, v81, s[8:9]
	v_cndmask_b32_e64 v81, v81, v85, s[8:9]
	ds_bpermute_b32 v81, v99, v81
	v_cndmask_b32_e64 v85, v83, v87, s[8:9]
	ds_bpermute_b32 v85, v99, v85
	v_and_b32_e32 v112, 16, v0
	v_cmp_eq_u32_e64 s[4:5], 0, v112
	s_waitcnt lgkmcnt(1)
	v_add_f32_e32 v80, v80, v81
	v_cndmask_b32_e64 v81, v86, v82, s[8:9]
	v_cndmask_b32_e64 v82, v87, v83, s[8:9]
	v_add_f32_e32 v81, v81, v84
	s_waitcnt lgkmcnt(0)
	v_add_f32_e32 v82, v82, v85
	v_add_f32_e64 v83, v114, |v50|
	v_cndmask_b32_e64 v84, v81, v79, s[4:5]
	v_cndmask_b32_e64 v79, v79, v81, s[4:5]
	v_cndmask_b32_e64 v81, v80, v82, s[4:5]
	ds_bpermute_b32 v79, v98, v79
	ds_bpermute_b32 v81, v98, v81
	v_add_f32_e64 v83, v83, |v51|
	v_add_f32_e64 v83, v83, |v52|
	v_cndmask_b32_e64 v80, v82, v80, s[4:5]
	v_add_f32_e64 v82, v83, |v53|
	ds_bpermute_b32 v83, v99, v82
	v_and_b32_e32 v113, 8, v0
	s_waitcnt lgkmcnt(2)
	v_add_f32_e32 v79, v84, v79
	s_waitcnt lgkmcnt(1)
	v_add_f32_e32 v80, v80, v81
	v_cmp_eq_u32_e64 s[6:7], 0, v113
	s_waitcnt lgkmcnt(0)
	v_add_f32_e32 v82, v82, v83
	ds_bpermute_b32 v83, v98, v82
	v_cndmask_b32_e64 v84, v80, v79, s[6:7]
	v_cndmask_b32_e64 v79, v79, v80, s[6:7]
	ds_bpermute_b32 v79, v97, v79
	v_cvt_pk_f16_f32 v81, v60, v61
	s_waitcnt lgkmcnt(1)
	v_add_f32_e32 v82, v82, v83
	ds_bpermute_b32 v83, v97, v82
	v_cvt_pk_f16_f32 v80, v58, v59
	s_waitcnt lgkmcnt(1)
	v_add_f32_e32 v79, v84, v79
	ds_bpermute_b32 v84, v96, v79
	global_store_dwordx2 v[76:77], v[80:81], off offset:512
	s_waitcnt lgkmcnt(1)
	v_add_f32_e32 v82, v82, v83
	ds_bpermute_b32 v83, v96, v82
	v_cvt_pk_f16_f32 v81, v56, v57
	s_waitcnt lgkmcnt(1)
	v_add_f32_e32 v79, v79, v84
	ds_bpermute_b32 v84, v75, v79
	v_cvt_pk_f16_f32 v80, v54, v55
	global_store_dwordx2 v[76:77], v[80:81], off offset:1024
	s_waitcnt lgkmcnt(1)
	v_add_f32_e32 v83, v82, v83
	ds_bpermute_b32 v86, v75, v83
	s_waitcnt lgkmcnt(1)
	v_add_f32_e32 v79, v79, v84
	ds_bpermute_b32 v80, v1, v79
	v_cvt_pk_f16_f32 v85, v52, v53
	v_cvt_pk_f16_f32 v84, v50, v51
	s_mov_b64 s[14:15], -1
	s_mov_b64 s[12:13], -1
	s_waitcnt lgkmcnt(0)
	v_add_f32_e32 v79, v79, v80
	s_waitcnt vmcnt(2)
	v_add_f32_e32 v81, v101, v79
	ds_bpermute_b32 v82, v97, v81
	v_add_f32_e32 v79, v83, v86
	ds_bpermute_b32 v80, v1, v79
	ds_bpermute_b32 v83, v97, v100
	global_store_dwordx2 v[76:77], v[84:85], off offset:1536
	s_waitcnt lgkmcnt(2)
	v_cmp_nlt_f32_e64 s[10:11], v81, v82
	s_and_saveexec_b64 s[16:17], s[10:11]
	s_cbranch_execz .LBB1_9
	v_cmp_eq_f32_e64 s[10:11], v81, v82
	s_waitcnt lgkmcnt(0)
	v_cmp_lt_i32_e64 s[12:13], v83, v100
	s_and_b64 s[10:11], s[10:11], s[12:13]
	s_orn2_b64 s[12:13], s[10:11], exec

.LBB1_45:
	s_or_b64 exec, exec, s[12:13]
	s_and_saveexec_b64 s[4:5], vcc
	ds_write_b32 v80, v18 offset:32780
	s_or_b64 exec, exec, s[4:5]
	v_cmp_gt_u32_e32 vcc, 8, v0
	s_waitcnt lgkmcnt(0)
	s_barrier
	s_and_saveexec_b64 s[54:55], vcc
	s_cbranch_execz .LBB1_89
	v_mov_b32_e32 v1, 0
	ds_read_b128 v[2:5], v1 offset:32768
	ds_read_b128 v[6:9], v1 offset:32784
	ds_read_b128 v[10:13], v1 offset:32800
	ds_read_b128 v[14:17], v1 offset:32816
	s_waitcnt lgkmcnt(3)
	v_cmp_eq_u32_e32 vcc, v3, v0
	s_waitcnt lgkmcnt(1)
	v_cmp_eq_u32_e64 s[48:49], v10, v0
	v_cndmask_b32_e64 v3, 0, 1, vcc
	v_cmp_eq_u32_e32 vcc, v2, v0
	v_cmp_eq_u32_e64 s[46:47], v11, v0
	v_cmp_eq_u32_e64 s[44:45], v12, v0
	v_addc_co_u32_e32 v2, vcc, 0, v3, vcc
	v_cmp_eq_u32_e32 vcc, v4, v0
	v_cmp_eq_u32_e64 s[42:43], v13, v0
	s_waitcnt lgkmcnt(0)
	v_cmp_eq_u32_e64 s[40:41], v14, v0
	v_cndmask_b32_e64 v3, 0, 1, vcc
	v_cmp_eq_u32_e32 vcc, v5, v0
	v_cmp_eq_u32_e64 s[38:39], v15, v0
	v_cmp_eq_u32_e64 s[36:37], v16, v0
	v_addc_co_u32_e32 v2, vcc, v2, v3, vcc
	v_cmp_eq_u32_e32 vcc, v6, v0
	v_cmp_eq_u32_e64 s[34:35], v17, v0
	s_nop 0
	v_cndmask_b32_e64 v3, 0, 1, vcc
	v_cmp_eq_u32_e32 vcc, v7, v0
	v_cndmask_b32_e64 v7, 0, 1, s[36:37]
	s_nop 0
	v_addc_co_u32_e32 v2, vcc, v2, v3, vcc
	v_cmp_eq_u32_e32 vcc, v8, v0
	s_nop 1
	v_cndmask_b32_e64 v3, 0, 1, vcc
	v_cmp_eq_u32_e32 vcc, v9, v0
	s_nop 1
	v_addc_co_u32_e32 v2, vcc, v2, v3, vcc
	v_cndmask_b32_e64 v3, 0, 1, s[48:49]
	v_addc_co_u32_e64 v2, vcc, v2, v3, s[46:47]
	v_cndmask_b32_e64 v3, 0, 1, s[44:45]
	v_addc_co_u32_e64 v2, vcc, v2, v3, s[42:43]
	v_cndmask_b32_e64 v3, 0, 1, s[40:41]
	v_addc_co_u32_e64 v6, vcc, v2, v3, s[38:39]
	ds_read_b128 v[2:5], v1 offset:32832
	v_addc_co_u32_e64 v10, vcc, v6, v7, s[34:35]
	ds_read_b128 v[6:9], v1 offset:32848
	s_waitcnt lgkmcnt(1)
	v_cmp_eq_u32_e64 s[30:31], v2, v0
	v_cmp_eq_u32_e64 s[28:29], v3, v0
	s_nop 0
	v_cndmask_b32_e64 v2, 0, 1, s[30:31]
	v_cmp_eq_u32_e64 s[26:27], v4, v0
	v_addc_co_u32_e64 v2, vcc, v10, v2, s[28:29]
	s_nop 0
	v_cndmask_b32_e64 v3, 0, 1, s[26:27]
	v_cmp_eq_u32_e64 s[24:25], v5, v0
	s_waitcnt lgkmcnt(0)
	v_cmp_eq_u32_e64 s[22:23], v6, v0
	v_cmp_eq_u32_e64 s[20:21], v7, v0
	v_addc_co_u32_e64 v2, vcc, v2, v3, s[24:25]
	v_cndmask_b32_e64 v3, 0, 1, s[22:23]
	v_addc_co_u32_e64 v6, vcc, v2, v3, s[20:21]
	v_cmp_eq_u32_e64 s[18:19], v8, v0
	ds_read_b128 v[2:5], v1 offset:32864
	v_cmp_eq_u32_e64 s[16:17], v9, v0
	v_cndmask_b32_e64 v7, 0, 1, s[18:19]
	s_nop 0
	v_addc_co_u32_e64 v10, vcc, v6, v7, s[16:17]
	ds_read_b128 v[6:9], v1 offset:32880
	s_waitcnt lgkmcnt(1)
	v_cmp_eq_u32_e64 s[14:15], v2, v0
	v_cmp_eq_u32_e64 s[12:13], v3, v0
	v_cmp_eq_u32_e64 s[10:11], v4, v0
	v_cndmask_b32_e64 v2, 0, 1, s[14:15]
	v_addc_co_u32_e64 v2, vcc, v10, v2, s[12:13]
	v_cndmask_b32_e64 v3, 0, 1, s[10:11]
	v_cmp_eq_u32_e64 s[8:9], v5, v0
	s_waitcnt lgkmcnt(0)
	v_cmp_eq_u32_e64 s[6:7], v6, v0
	v_cmp_eq_u32_e64 s[4:5], v7, v0
	v_addc_co_u32_e64 v2, vcc, v2, v3, s[8:9]
	v_cndmask_b32_e64 v3, 0, 1, s[6:7]
	v_addc_co_u32_e64 v2, vcc, v2, v3, s[4:5]
	v_cmp_eq_u32_e64 s[50:51], v8, v0
	v_cmp_eq_u32_e32 vcc, v9, v0
	s_nop 0
	v_cndmask_b32_e64 v3, 0, 1, s[50:51]
	v_addc_co_u32_e64 v2, s[52:53], v2, v3, vcc
	v_cmp_ne_u32_e64 s[52:53], 0, v2
	s_and_b64 exec, exec, s[52:53]
	s_cbranch_execz .LBB1_89
	v_lshlrev_b32_e32 v3, 7, v0
	global_atomic_add v2, v3, v2, s[56:57] sc0
	ds_read_b32 v3, v1 offset:32768
	v_lshlrev_b32_e32 v1, 13, v0
	s_lshl_b32 s3, s2, 5
	s_waitcnt vmcnt(0) lgkmcnt(0)
	v_cmp_eq_u32_e64 s[52:53], v3, v0
	s_and_saveexec_b64 s[56:57], s[52:53]
	s_cbranch_execz .LBB1_51
	v_add_u32_e32 v4, 1, v2
	v_add_u32_e32 v2, v2, v1
	v_ashrrev_i32_e32 v3, 31, v2
	v_lshl_add_u64 v[2:3], v[2:3], 2, s[58:59]
	v_mov_b32_e32 v5, s3
	global_store_dword v[2:3], v5, off
	v_mov_b32_e32 v2, v4
.LBB1_51:
	s_or_b64 exec, exec, s[56:57]
	v_mov_b32_e32 v3, 0
	ds_read_b32 v4, v3 offset:32772
	s_waitcnt lgkmcnt(0)
	v_cmp_eq_u32_e64 s[52:53], v4, v0
	s_and_saveexec_b64 s[56:57], s[52:53]
	s_cbranch_execz .LBB1_53
	v_add_u32_e32 v4, v2, v1
	v_ashrrev_i32_e32 v5, 31, v4
	s_or_b32 s33, s3, 1
	v_add_u32_e32 v6, 1, v2
	v_lshl_add_u64 v[4:5], v[4:5], 2, s[58:59]
	v_mov_b32_e32 v2, s33
	global_store_dword v[4:5], v2, off
	v_mov_b32_e32 v2, v6
.LBB1_53:
	s_or_b64 exec, exec, s[56:57]
	ds_read_b32 v3, v3 offset:32776
	s_waitcnt lgkmcnt(0)
	v_cmp_eq_u32_e64 s[52:53], v3, v0
	s_and_saveexec_b64 s[56:57], s[52:53]
	s_cbranch_execz .LBB1_55
	v_add_u32_e32 v4, 1, v2
	v_add_u32_e32 v2, v2, v1
	v_ashrrev_i32_e32 v3, 31, v2
	s_or_b32 s33, s3, 2
	v_lshl_add_u64 v[2:3], v[2:3], 2, s[58:59]
	v_mov_b32_e32 v5, s33
	global_store_dword v[2:3], v5, off
	v_mov_b32_e32 v2, v4
.LBB1_55:
	s_or_b64 exec, exec, s[56:57]
	v_mov_b32_e32 v3, 0
	ds_read_b32 v4, v3 offset:32780
	s_waitcnt lgkmcnt(0)
	v_cmp_eq_u32_e64 s[52:53], v4, v0
	s_and_saveexec_b64 s[56:57], s[52:53]
	s_cbranch_execz .LBB1_57
	v_add_u32_e32 v4, v2, v1
	v_ashrrev_i32_e32 v5, 31, v4
	s_or_b32 s33, s3, 3
	v_add_u32_e32 v6, 1, v2
	v_lshl_add_u64 v[4:5], v[4:5], 2, s[58:59]
	v_mov_b32_e32 v2, s33
	global_store_dword v[4:5], v2, off
	v_mov_b32_e32 v2, v6
.LBB1_57:
	s_or_b64 exec, exec, s[56:57]
	ds_read_b32 v3, v3 offset:32784
	s_waitcnt lgkmcnt(0)
	v_cmp_eq_u32_e64 s[52:53], v3, v0
	s_and_saveexec_b64 s[56:57], s[52:53]
	s_cbranch_execz .LBB1_59
	v_add_u32_e32 v4, 1, v2
	v_add_u32_e32 v2, v2, v1
	v_ashrrev_i32_e32 v3, 31, v2
	s_or_b32 s33, s3, 4
	v_lshl_add_u64 v[2:3], v[2:3], 2, s[58:59]
	v_mov_b32_e32 v5, s33
	global_store_dword v[2:3], v5, off
	v_mov_b32_e32 v2, v4
.LBB1_59:
	s_or_b64 exec, exec, s[56:57]
	v_mov_b32_e32 v3, 0
	ds_read_b32 v4, v3 offset:32788
	s_waitcnt lgkmcnt(0)
	v_cmp_eq_u32_e64 s[52:53], v4, v0
	s_and_saveexec_b64 s[56:57], s[52:53]
	s_cbranch_execz .LBB1_61
	v_add_u32_e32 v4, v2, v1
	v_ashrrev_i32_e32 v5, 31, v4
	s_or_b32 s33, s3, 5
	v_add_u32_e32 v6, 1, v2
	v_lshl_add_u64 v[4:5], v[4:5], 2, s[58:59]
	v_mov_b32_e32 v2, s33
	global_store_dword v[4:5], v2, off
	v_mov_b32_e32 v2, v6
.LBB1_61:
	s_or_b64 exec, exec, s[56:57]
	ds_read_b32 v3, v3 offset:32792
	s_waitcnt lgkmcnt(0)
	v_cmp_eq_u32_e64 s[52:53], v3, v0
	s_and_saveexec_b64 s[56:57], s[52:53]
	s_cbranch_execz .LBB1_63
	v_add_u32_e32 v4, 1, v2
	v_add_u32_e32 v2, v2, v1
	v_ashrrev_i32_e32 v3, 31, v2
	s_or_b32 s33, s3, 6
	v_lshl_add_u64 v[2:3], v[2:3], 2, s[58:59]
	v_mov_b32_e32 v5, s33
	global_store_dword v[2:3], v5, off
	v_mov_b32_e32 v2, v4

.LBB1_88:
	v_add_u32_e32 v2, v2, v1
	v_ashrrev_i32_e32 v3, 31, v2
	s_or_b32 s3, s3, 31
	v_lshl_add_u64 v[2:3], v[2:3], 2, s[58:59]
	v_mov_b32_e32 v1, s3
	global_store_dword v[2:3], v1, off

.LBB1_95:
	v_add_u32_e32 v4, 1, v2
	v_add_u32_e32 v2, v2, v1
	v_ashrrev_i32_e32 v3, 31, v2
	s_or_b32 s33, s3, 7
	v_lshl_add_u64 v[2:3], v[2:3], 2, s[58:59]
	v_mov_b32_e32 v5, s33
	global_store_dword v[2:3], v5, off
	v_mov_b32_e32 v2, v4
	s_or_b64 exec, exec, s[56:57]
	s_and_saveexec_b64 s[52:53], s[48:49]
	s_cbranch_execz .LBB1_65
.LBB1_96:
	v_add_u32_e32 v4, 1, v2
	v_add_u32_e32 v2, v2, v1
	v_ashrrev_i32_e32 v3, 31, v2
	s_or_b32 s33, s3, 8
	v_lshl_add_u64 v[2:3], v[2:3], 2, s[58:59]
	v_mov_b32_e32 v5, s33
	global_store_dword v[2:3], v5, off
	v_mov_b32_e32 v2, v4
	s_or_b64 exec, exec, s[52:53]
	s_and_saveexec_b64 s[48:49], s[46:47]
	s_cbranch_execz .LBB1_66
.LBB1_97:
	v_add_u32_e32 v4, 1, v2
	v_add_u32_e32 v2, v2, v1
	v_ashrrev_i32_e32 v3, 31, v2
	s_or_b32 s33, s3, 9
	v_lshl_add_u64 v[2:3], v[2:3], 2, s[58:59]
	v_mov_b32_e32 v5, s33
	global_store_dword v[2:3], v5, off
	v_mov_b32_e32 v2, v4
	s_or_b64 exec, exec, s[48:49]
	s_and_saveexec_b64 s[46:47], s[44:45]
	s_cbranch_execz .LBB1_67
.LBB1_98:
	v_add_u32_e32 v4, 1, v2
	v_add_u32_e32 v2, v2, v1
	v_ashrrev_i32_e32 v3, 31, v2
	s_or_b32 s33, s3, 10
	v_lshl_add_u64 v[2:3], v[2:3], 2, s[58:59]
	v_mov_b32_e32 v5, s33
	global_store_dword v[2:3], v5, off
	v_mov_b32_e32 v2, v4
	s_or_b64 exec, exec, s[46:47]
	s_and_saveexec_b64 s[44:45], s[42:43]
	s_cbranch_execz .LBB1_68
.LBB1_99:
	v_add_u32_e32 v4, 1, v2
	v_add_u32_e32 v2, v2, v1
	v_ashrrev_i32_e32 v3, 31, v2
	s_or_b32 s33, s3, 11
	v_lshl_add_u64 v[2:3], v[2:3], 2, s[58:59]
	v_mov_b32_e32 v5, s33
	global_store_dword v[2:3], v5, off
	v_mov_b32_e32 v2, v4
	s_or_b64 exec, exec, s[44:45]
	s_and_saveexec_b64 s[42:43], s[40:41]
	s_cbranch_execz .LBB1_69
.LBB1_100:
	v_add_u32_e32 v4, 1, v2
	v_add_u32_e32 v2, v2, v1
	v_ashrrev_i32_e32 v3, 31, v2
	s_or_b32 s33, s3, 12
	v_lshl_add_u64 v[2:3], v[2:3], 2, s[58:59]
	v_mov_b32_e32 v5, s33
	global_store_dword v[2:3], v5, off
	v_mov_b32_e32 v2, v4
	s_or_b64 exec, exec, s[42:43]
	s_and_saveexec_b64 s[40:41], s[38:39]
	s_cbranch_execz .LBB1_70
.LBB1_101:
	v_add_u32_e32 v4, 1, v2
	v_add_u32_e32 v2, v2, v1
	v_ashrrev_i32_e32 v3, 31, v2
	s_or_b32 s33, s3, 13
	v_lshl_add_u64 v[2:3], v[2:3], 2, s[58:59]
	v_mov_b32_e32 v5, s33
	global_store_dword v[2:3], v5, off
	v_mov_b32_e32 v2, v4
	s_or_b64 exec, exec, s[40:41]
	s_and_saveexec_b64 s[38:39], s[36:37]
	s_cbranch_execz .LBB1_71
.LBB1_102:
	v_add_u32_e32 v4, 1, v2
	v_add_u32_e32 v2, v2, v1
	v_ashrrev_i32_e32 v3, 31, v2
	s_or_b32 s33, s3, 14
	v_lshl_add_u64 v[2:3], v[2:3], 2, s[58:59]
	v_mov_b32_e32 v5, s33
	global_store_dword v[2:3], v5, off
	v_mov_b32_e32 v2, v4
	s_or_b64 exec, exec, s[38:39]
	s_and_saveexec_b64 s[36:37], s[34:35]
	s_cbranch_execz .LBB1_72
.LBB1_103:
	v_add_u32_e32 v4, 1, v2
	v_add_u32_e32 v2, v2, v1
	v_ashrrev_i32_e32 v3, 31, v2
	s_or_b32 s33, s3, 15
	v_lshl_add_u64 v[2:3], v[2:3], 2, s[58:59]
	v_mov_b32_e32 v5, s33
	global_store_dword v[2:3], v5, off
	v_mov_b32_e32 v2, v4
	s_or_b64 exec, exec, s[36:37]
	s_and_saveexec_b64 s[34:35], s[30:31]
	s_cbranch_execz .LBB1_73
.LBB1_104:
	v_add_u32_e32 v4, 1, v2
	v_add_u32_e32 v2, v2, v1
	v_ashrrev_i32_e32 v3, 31, v2
	s_or_b32 s30, s3, 16
	v_lshl_add_u64 v[2:3], v[2:3], 2, s[58:59]
	v_mov_b32_e32 v5, s30
	global_store_dword v[2:3], v5, off
	v_mov_b32_e32 v2, v4
	s_or_b64 exec, exec, s[34:35]
	s_and_saveexec_b64 s[30:31], s[28:29]
	s_cbranch_execz .LBB1_74
.LBB1_105:
	v_add_u32_e32 v4, 1, v2
	v_add_u32_e32 v2, v2, v1
	v_ashrrev_i32_e32 v3, 31, v2
	s_or_b32 s28, s3, 17
	v_lshl_add_u64 v[2:3], v[2:3], 2, s[58:59]
	v_mov_b32_e32 v5, s28
	global_store_dword v[2:3], v5, off
	v_mov_b32_e32 v2, v4
	s_or_b64 exec, exec, s[30:31]
	s_and_saveexec_b64 s[28:29], s[26:27]
	s_cbranch_execz .LBB1_75
.LBB1_106:
	v_add_u32_e32 v4, 1, v2
	v_add_u32_e32 v2, v2, v1
	v_ashrrev_i32_e32 v3, 31, v2
	s_or_b32 s26, s3, 18
	v_lshl_add_u64 v[2:3], v[2:3], 2, s[58:59]
	v_mov_b32_e32 v5, s26
	global_store_dword v[2:3], v5, off
	v_mov_b32_e32 v2, v4
	s_or_b64 exec, exec, s[28:29]
	s_and_saveexec_b64 s[26:27], s[24:25]
	s_cbranch_execz .LBB1_76
.LBB1_107:
	v_add_u32_e32 v4, 1, v2
	v_add_u32_e32 v2, v2, v1
	v_ashrrev_i32_e32 v3, 31, v2
	s_or_b32 s24, s3, 19
	v_lshl_add_u64 v[2:3], v[2:3], 2, s[58:59]
	v_mov_b32_e32 v5, s24
	global_store_dword v[2:3], v5, off
	v_mov_b32_e32 v2, v4
	s_or_b64 exec, exec, s[26:27]
	s_and_saveexec_b64 s[24:25], s[22:23]
	s_cbranch_execz .LBB1_77
.LBB1_108:
	v_add_u32_e32 v4, 1, v2
	v_add_u32_e32 v2, v2, v1
	v_ashrrev_i32_e32 v3, 31, v2
	s_or_b32 s22, s3, 20
	v_lshl_add_u64 v[2:3], v[2:3], 2, s[58:59]
	v_mov_b32_e32 v5, s22
	global_store_dword v[2:3], v5, off
	v_mov_b32_e32 v2, v4
	s_or_b64 exec, exec, s[24:25]
	s_and_saveexec_b64 s[22:23], s[20:21]
	s_cbranch_execz .LBB1_78
.LBB1_109:
	v_add_u32_e32 v4, 1, v2
	v_add_u32_e32 v2, v2, v1
	v_ashrrev_i32_e32 v3, 31, v2
	s_or_b32 s20, s3, 21
	v_lshl_add_u64 v[2:3], v[2:3], 2, s[58:59]
	v_mov_b32_e32 v5, s20
	global_store_dword v[2:3], v5, off
	v_mov_b32_e32 v2, v4
	s_or_b64 exec, exec, s[22:23]
	s_and_saveexec_b64 s[20:21], s[18:19]
	s_cbranch_execz .LBB1_79
.LBB1_110:
	v_add_u32_e32 v4, 1, v2
	v_add_u32_e32 v2, v2, v1
	v_ashrrev_i32_e32 v3, 31, v2
	s_or_b32 s18, s3, 22
	v_lshl_add_u64 v[2:3], v[2:3], 2, s[58:59]
	v_mov_b32_e32 v5, s18
	global_store_dword v[2:3], v5, off
	v_mov_b32_e32 v2, v4
	s_or_b64 exec, exec, s[20:21]
	s_and_saveexec_b64 s[18:19], s[16:17]
	s_cbranch_execz .LBB1_80
.LBB1_111:
	v_add_u32_e32 v4, 1, v2
	v_add_u32_e32 v2, v2, v1
	v_ashrrev_i32_e32 v3, 31, v2
	s_or_b32 s16, s3, 23
	v_lshl_add_u64 v[2:3], v[2:3], 2, s[58:59]
	v_mov_b32_e32 v5, s16
	global_store_dword v[2:3], v5, off
	v_mov_b32_e32 v2, v4
	s_or_b64 exec, exec, s[18:19]
	s_and_saveexec_b64 s[16:17], s[14:15]
	s_cbranch_execz .LBB1_81
.LBB1_112:
	v_add_u32_e32 v4, 1, v2
	v_add_u32_e32 v2, v2, v1
	v_ashrrev_i32_e32 v3, 31, v2
	s_or_b32 s14, s3, 24
	v_lshl_add_u64 v[2:3], v[2:3], 2, s[58:59]
	v_mov_b32_e32 v5, s14
	global_store_dword v[2:3], v5, off
	v_mov_b32_e32 v2, v4
	s_or_b64 exec, exec, s[16:17]
	s_and_saveexec_b64 s[14:15], s[12:13]
	s_cbranch_execz .LBB1_82
.LBB1_113:
	v_add_u32_e32 v4, 1, v2
	v_add_u32_e32 v2, v2, v1
	v_ashrrev_i32_e32 v3, 31, v2
	s_or_b32 s12, s3, 25
	v_lshl_add_u64 v[2:3], v[2:3], 2, s[58:59]
	v_mov_b32_e32 v5, s12
	global_store_dword v[2:3], v5, off
	v_mov_b32_e32 v2, v4
	s_or_b64 exec, exec, s[14:15]
	s_and_saveexec_b64 s[12:13], s[10:11]
	s_cbranch_execz .LBB1_83
.LBB1_114:
	v_add_u32_e32 v4, 1, v2
	v_add_u32_e32 v2, v2, v1
	v_ashrrev_i32_e32 v3, 31, v2
	s_or_b32 s10, s3, 26
	v_lshl_add_u64 v[2:3], v[2:3], 2, s[58:59]
	v_mov_b32_e32 v5, s10
	global_store_dword v[2:3], v5, off
	v_mov_b32_e32 v2, v4
	s_or_b64 exec, exec, s[12:13]
	s_and_saveexec_b64 s[10:11], s[8:9]
	s_cbranch_execz .LBB1_84
.LBB1_115:
	v_add_u32_e32 v4, 1, v2
	v_add_u32_e32 v2, v2, v1
	v_ashrrev_i32_e32 v3, 31, v2
	s_or_b32 s8, s3, 27
	v_lshl_add_u64 v[2:3], v[2:3], 2, s[58:59]
	v_mov_b32_e32 v5, s8
	global_store_dword v[2:3], v5, off
	v_mov_b32_e32 v2, v4
	s_or_b64 exec, exec, s[10:11]
	s_and_saveexec_b64 s[8:9], s[6:7]
	s_cbranch_execz .LBB1_85
.LBB1_116:
	v_add_u32_e32 v4, 1, v2
	v_add_u32_e32 v2, v2, v1
	v_ashrrev_i32_e32 v3, 31, v2
	s_or_b32 s6, s3, 28
	v_lshl_add_u64 v[2:3], v[2:3], 2, s[58:59]
	v_mov_b32_e32 v5, s6
	global_store_dword v[2:3], v5, off
	v_mov_b32_e32 v2, v4
	s_or_b64 exec, exec, s[8:9]
	s_and_saveexec_b64 s[6:7], s[4:5]
	s_cbranch_execz .LBB1_86
.LBB1_117:
	v_add_u32_e32 v4, 1, v2
	v_add_u32_e32 v2, v2, v1
	v_ashrrev_i32_e32 v3, 31, v2
	s_or_b32 s4, s3, 29
	v_lshl_add_u64 v[2:3], v[2:3], 2, s[58:59]
	v_mov_b32_e32 v5, s4
	global_store_dword v[2:3], v5, off
	v_mov_b32_e32 v2, v4
	s_or_b64 exec, exec, s[6:7]
	s_and_saveexec_b64 s[4:5], s[50:51]
	s_cbranch_execz .LBB1_87
.LBB1_118:
	v_add_u32_e32 v4, 1, v2
	v_add_u32_e32 v2, v2, v1
	v_ashrrev_i32_e32 v3, 31, v2
	s_or_b32 s6, s3, 30
	v_lshl_add_u64 v[2:3], v[2:3], 2, s[58:59]
	v_mov_b32_e32 v5, s6
	global_store_dword v[2:3], v5, off
	v_mov_b32_e32 v2, v4
	s_or_b64 exec, exec, s[4:5]
	s_and_b64 exec, exec, vcc
	s_cbranch_execnz .LBB1_88
	s_branch .LBB1_89
